# speedup vs baseline: 1.0039x; 1.0039x over previous
.Lc_wait0:
	ds_read_b32 v37, v36
	ds_read_b32 v38, v36 offset:64
	s_waitcnt lgkmcnt(0)
	v_readfirstlane_b32 s4, v37
	v_readfirstlane_b32 s5, v38
	s_and_b32 s4, s4, s5
	s_cbranch_scc1 .Lc_go
	s_sleep 3
	s_add_i32 s73, s73, 1
	s_cmp_lt_u32 s73, 0x4000
	s_cbranch_scc1 .Lc_wait0

.Lc0_fin:
	ds_read_b32 v45, v36 offset:128
	s_waitcnt lgkmcnt(0)
	v_readfirstlane_b32 s4, v45
	s_cmp_eq_u32 s4, 4
	s_cbranch_scc1 .Lc0_fin2
	s_sleep 3
	s_add_i32 s73, s73, 1
	s_cmp_lt_u32 s73, 0x4000
	s_cbranch_scc1 .Lc0_fin

.Lc0_slow0:
	s_sleep 3
	ds_read_b32 v37, v36 offset:4
	ds_read_b32 v38, v36 offset:68
	s_waitcnt lgkmcnt(0)
	v_readfirstlane_b32 s4, v37
	v_readfirstlane_b32 s5, v38
	s_and_b32 s4, s4, s5
	s_cbranch_scc1 .Lc0_back0
	s_add_i32 s73, s73, 1
	s_cmp_lt_u32 s73, 0x4000
	s_cbranch_scc1 .Lc0_slow0
	s_branch .Lc0_back0
.Lc0_slow1:
	s_sleep 3
	ds_read_b32 v37, v36 offset:8
	ds_read_b32 v38, v36 offset:72
	s_waitcnt lgkmcnt(0)
	v_readfirstlane_b32 s4, v37
	v_readfirstlane_b32 s5, v38
	s_and_b32 s4, s4, s5
	s_cbranch_scc1 .Lc0_back1
	s_add_i32 s73, s73, 1
	s_cmp_lt_u32 s73, 0x4000
	s_cbranch_scc1 .Lc0_slow1
	s_branch .Lc0_back1

.Lc1_dslow0:
	s_sleep 3
	ds_read_b32 v45, v36 offset:124
	s_waitcnt lgkmcnt(0)
	v_readfirstlane_b32 s4, v45
	s_cmp_eq_u32 s4, 4
	s_cbranch_scc1 .Lc1_dgo0
	s_add_i32 s73, s73, 1
	s_cmp_lt_u32 s73, 0x4000
	s_cbranch_scc1 .Lc1_dslow0

.Lc1_dslow1:
	s_sleep 3
	ds_read_b32 v45, v36 offset:128
	s_waitcnt lgkmcnt(0)
	v_readfirstlane_b32 s4, v45
	s_cmp_eq_u32 s4, 4
	s_cbranch_scc1 .Lc1_dgo1
	s_add_i32 s73, s73, 1
	s_cmp_lt_u32 s73, 0x4000
	s_cbranch_scc1 .Lc1_dslow1
